# s12p + prep_phase conv-weight LDS fill: 5 trips x 4 dword loads all in flight before counted-vmcnt LDS writes (L0 and L1); padded
# speedup vs baseline: 1.0053x; 1.0053x over previous
; DI void prep_phase(const Params& P, const Frame& F, int L) {
;     ...
;     for (int i = F.tid; i < 4 * 2560; i += NTHR) { const int tap = i / 2560, ch = i % 2560;
;         CW[i] = ch < 1536 ? P.in[I_CONV_DN][(size_t)(L * 4 + tap) * 1536 + ch] : P.in[I_CONV_ML][(size_t)(L * 4 + tap) * 1024 + ch - 1536]; }
.LBB0_296:
	v_mul_hi_i32 v8, v0, s14
	v_mul_hi_i32 v9, v1, s14
	v_add_u32_e32 v28, 0x400, v1
	v_add_u32_e32 v29, 0x400, v0
	v_lshrrev_b32_e32 v10, 31, v8
	v_ashrrev_i32_e32 v8, 10, v8
	v_lshrrev_b32_e32 v11, 31, v9
	v_ashrrev_i32_e32 v9, 10, v9
	v_mul_hi_i32 v12, v29, s14
	v_mul_hi_i32 v13, v28, s14
	v_add_u32_e32 v8, v8, v10
	v_add_u32_e32 v10, v9, v11
	v_lshrrev_b32_e32 v16, 31, v12
	v_ashrrev_i32_e32 v17, 10, v12
	v_lshrrev_b32_e32 v18, 31, v13
	v_ashrrev_i32_e32 v19, 10, v13
	v_mul_i32_i24_e32 v21, 0xa00, v8
	v_mul_i32_i24_e32 v20, 0xa00, v10
	v_add_u32_e32 v16, v17, v16
	v_add_u32_e32 v18, v19, v18
	v_ashrrev_i32_e32 v9, 31, v8
	v_ashrrev_i32_e32 v11, 31, v10
	v_sub_u32_e32 v20, v1, v20
	v_sub_u32_e32 v22, v0, v21
	v_mul_i32_i24_e32 v30, 0xa00, v16
	v_mul_i32_i24_e32 v31, 0xa00, v18
	v_mad_i64_i32 v[12:13], s[4:5], v10, s16, v[2:3]
	v_mad_i64_i32 v[14:15], s[4:5], v8, s16, v[2:3]
	v_lshlrev_b64 v[10:11], 12, v[10:11]
	v_lshlrev_b64 v[8:9], 12, v[8:9]
	v_ashrrev_i32_e32 v17, 31, v16
	v_ashrrev_i32_e32 v19, 31, v18
	v_ashrrev_i32_e32 v21, 31, v20
	v_ashrrev_i32_e32 v23, 31, v22
	v_sub_u32_e32 v28, v28, v31
	v_sub_u32_e32 v30, v29, v30
	v_mad_i64_i32 v[24:25], s[4:5], v18, s16, v[2:3]
	v_mad_i64_i32 v[26:27], s[4:5], v16, s16, v[2:3]
	v_lshl_add_u64 v[8:9], s[78:79], 0, v[8:9]
	v_lshl_add_u64 v[10:11], s[78:79], 0, v[10:11]
	v_lshlrev_b64 v[18:19], 12, v[18:19]
	v_lshlrev_b64 v[16:17], 12, v[16:17]
	s_waitcnt vmcnt(15)
	v_lshlrev_b64 v[32:33], 2, v[20:21]
	v_lshlrev_b64 v[34:35], 2, v[22:23]
	v_ashrrev_i32_e32 v29, 31, v28
	v_ashrrev_i32_e32 v31, 31, v30
	v_lshl_add_u64 v[16:17], s[78:79], 0, v[16:17]
	v_lshl_add_u64 v[18:19], s[78:79], 0, v[18:19]
	v_lshl_add_u64 v[10:11], v[10:11], 0, v[32:33]
	v_lshl_add_u64 v[8:9], v[8:9], 0, v[34:35]
	v_lshl_add_u64 v[14:15], v[14:15], 0, v[34:35]
	v_lshl_add_u64 v[12:13], v[12:13], 0, v[32:33]
	v_lshlrev_b64 v[32:33], 2, v[28:29]
	v_lshlrev_b64 v[34:35], 2, v[30:31]
	v_lshl_add_u64 v[8:9], v[8:9], 0, s[12:13]
	v_cmp_gt_i32_e32 vcc, s15, v22
	v_lshl_add_u64 v[10:11], v[10:11], 0, s[12:13]
	v_lshl_add_u64 v[18:19], v[18:19], 0, v[32:33]
	v_lshl_add_u64 v[16:17], v[16:17], 0, v[34:35]
	v_cmp_gt_i32_e64 s[4:5], s15, v20
	v_lshl_add_u64 v[22:23], v[26:27], 0, v[34:35]
	v_lshl_add_u64 v[24:25], v[24:25], 0, v[32:33]
	v_cndmask_b32_e64 v11, v11, v13, s[4:5]
	v_cndmask_b32_e64 v10, v10, v12, s[4:5]
	v_cndmask_b32_e32 v9, v9, v15, vcc
	v_cndmask_b32_e32 v8, v8, v14, vcc
	v_lshl_add_u64 v[12:13], v[16:17], 0, s[12:13]
	v_cmp_gt_i32_e32 vcc, s15, v30
	v_lshl_add_u64 v[14:15], v[18:19], 0, s[12:13]
	v_cmp_gt_i32_e64 s[4:5], s15, v28
	global_load_dword v186, v[8:9], off
	global_load_dword v187, v[10:11], off
	v_cndmask_b32_e64 v9, v15, v25, s[4:5]
	v_cndmask_b32_e32 v11, v13, v23, vcc
	v_cndmask_b32_e32 v10, v12, v22, vcc
	v_cndmask_b32_e64 v8, v14, v24, s[4:5]
	global_load_dword v188, v[10:11], off
	s_nop 0
	global_load_dword v189, v[8:9], off
	v_add_u32_e32 v6, -2, v6
	s_add_i32 s3, s3, 4
	v_cmp_eq_u32_e32 vcc, 0, v6
	v_mov_b32_e32 v8, s3
	s_or_b64 s[10:11], vcc, s[10:11]
	v_add_u32_e32 v1, 0x800, v1
	v_add_u32_e32 v0, 0x800, v0
	v_mul_hi_i32 v8, v0, s14
	v_mul_hi_i32 v9, v1, s14
	v_add_u32_e32 v28, 0x400, v1
	v_add_u32_e32 v29, 0x400, v0
	v_lshrrev_b32_e32 v10, 31, v8
	v_ashrrev_i32_e32 v8, 10, v8
	v_lshrrev_b32_e32 v11, 31, v9
	v_ashrrev_i32_e32 v9, 10, v9
	v_mul_hi_i32 v12, v29, s14
	v_mul_hi_i32 v13, v28, s14
	v_add_u32_e32 v8, v8, v10
	v_add_u32_e32 v10, v9, v11
	v_lshrrev_b32_e32 v16, 31, v12
	v_ashrrev_i32_e32 v17, 10, v12
	v_lshrrev_b32_e32 v18, 31, v13
	v_ashrrev_i32_e32 v19, 10, v13
	v_mul_i32_i24_e32 v21, 0xa00, v8
	v_mul_i32_i24_e32 v20, 0xa00, v10
	v_add_u32_e32 v16, v17, v16
	v_add_u32_e32 v18, v19, v18
	v_ashrrev_i32_e32 v9, 31, v8
	v_ashrrev_i32_e32 v11, 31, v10
	v_sub_u32_e32 v20, v1, v20
	v_sub_u32_e32 v22, v0, v21
	v_mul_i32_i24_e32 v30, 0xa00, v16
	v_mul_i32_i24_e32 v31, 0xa00, v18
	v_mad_i64_i32 v[12:13], s[4:5], v10, s16, v[2:3]
	v_mad_i64_i32 v[14:15], s[4:5], v8, s16, v[2:3]
	v_lshlrev_b64 v[10:11], 12, v[10:11]
	v_lshlrev_b64 v[8:9], 12, v[8:9]
	v_ashrrev_i32_e32 v17, 31, v16
	v_ashrrev_i32_e32 v19, 31, v18
	v_ashrrev_i32_e32 v21, 31, v20
	v_ashrrev_i32_e32 v23, 31, v22
	v_sub_u32_e32 v28, v28, v31
	v_sub_u32_e32 v30, v29, v30
	v_mad_i64_i32 v[24:25], s[4:5], v18, s16, v[2:3]
	v_mad_i64_i32 v[26:27], s[4:5], v16, s16, v[2:3]
	v_lshl_add_u64 v[8:9], s[78:79], 0, v[8:9]
	v_lshl_add_u64 v[10:11], s[78:79], 0, v[10:11]
	v_lshlrev_b64 v[18:19], 12, v[18:19]
	v_lshlrev_b64 v[16:17], 12, v[16:17]
	v_lshlrev_b64 v[32:33], 2, v[20:21]
	v_lshlrev_b64 v[34:35], 2, v[22:23]
	v_ashrrev_i32_e32 v29, 31, v28
	v_ashrrev_i32_e32 v31, 31, v30
	v_lshl_add_u64 v[16:17], s[78:79], 0, v[16:17]
	v_lshl_add_u64 v[18:19], s[78:79], 0, v[18:19]
	v_lshl_add_u64 v[10:11], v[10:11], 0, v[32:33]
	v_lshl_add_u64 v[8:9], v[8:9], 0, v[34:35]
	v_lshl_add_u64 v[14:15], v[14:15], 0, v[34:35]
	v_lshl_add_u64 v[12:13], v[12:13], 0, v[32:33]
	v_lshlrev_b64 v[32:33], 2, v[28:29]
	v_lshlrev_b64 v[34:35], 2, v[30:31]
	v_lshl_add_u64 v[8:9], v[8:9], 0, s[12:13]
	v_cmp_gt_i32_e32 vcc, s15, v22
	v_lshl_add_u64 v[10:11], v[10:11], 0, s[12:13]
	v_lshl_add_u64 v[18:19], v[18:19], 0, v[32:33]
	v_lshl_add_u64 v[16:17], v[16:17], 0, v[34:35]
	v_cmp_gt_i32_e64 s[4:5], s15, v20
	v_lshl_add_u64 v[22:23], v[26:27], 0, v[34:35]
	v_lshl_add_u64 v[24:25], v[24:25], 0, v[32:33]
	v_cndmask_b32_e64 v11, v11, v13, s[4:5]
	v_cndmask_b32_e64 v10, v10, v12, s[4:5]
	v_cndmask_b32_e32 v9, v9, v15, vcc
	v_cndmask_b32_e32 v8, v8, v14, vcc
	v_lshl_add_u64 v[12:13], v[16:17], 0, s[12:13]
	v_cmp_gt_i32_e32 vcc, s15, v30
	v_lshl_add_u64 v[14:15], v[18:19], 0, s[12:13]
; DI void prep_phase(const Params& P, const Frame& F, int L) {
;     ...
;     for (int i = F.tid; i < 4 * 2560; i += NTHR) { const int tap = i / 2560, ch = i % 2560;
;         CW[i] = ch < 1536 ? P.in[I_CONV_DN][(size_t)(L * 4 + tap) * 1536 + ch] : P.in[I_CONV_ML][(size_t)(L * 4 + tap) * 1024 + ch - 1536]; }
	v_cmp_gt_i32_e64 s[4:5], s15, v28
	global_load_dword v190, v[8:9], off
	global_load_dword v191, v[10:11], off
	v_cndmask_b32_e64 v9, v15, v25, s[4:5]
	v_cndmask_b32_e32 v11, v13, v23, vcc
	v_cndmask_b32_e32 v10, v12, v22, vcc
	v_cndmask_b32_e64 v8, v14, v24, s[4:5]
	global_load_dword v192, v[10:11], off
	s_nop 0
	global_load_dword v193, v[8:9], off
	v_add_u32_e32 v6, -2, v6
	s_add_i32 s3, s3, 4
	v_cmp_eq_u32_e32 vcc, 0, v6
	v_mov_b32_e32 v8, s3
	s_or_b64 s[10:11], vcc, s[10:11]
	v_add_u32_e32 v1, 0x800, v1
	v_add_u32_e32 v0, 0x800, v0
	v_mul_hi_i32 v8, v0, s14
	v_mul_hi_i32 v9, v1, s14
	v_add_u32_e32 v28, 0x400, v1
	v_add_u32_e32 v29, 0x400, v0
	v_lshrrev_b32_e32 v10, 31, v8
	v_ashrrev_i32_e32 v8, 10, v8
	v_lshrrev_b32_e32 v11, 31, v9
	v_ashrrev_i32_e32 v9, 10, v9
	v_mul_hi_i32 v12, v29, s14
	v_mul_hi_i32 v13, v28, s14
	v_add_u32_e32 v8, v8, v10
	v_add_u32_e32 v10, v9, v11
	v_lshrrev_b32_e32 v16, 31, v12
	v_ashrrev_i32_e32 v17, 10, v12
	v_lshrrev_b32_e32 v18, 31, v13
	v_ashrrev_i32_e32 v19, 10, v13
	v_mul_i32_i24_e32 v21, 0xa00, v8
	v_mul_i32_i24_e32 v20, 0xa00, v10
	v_add_u32_e32 v16, v17, v16
	v_add_u32_e32 v18, v19, v18
	v_ashrrev_i32_e32 v9, 31, v8
	v_ashrrev_i32_e32 v11, 31, v10
	v_sub_u32_e32 v20, v1, v20
	v_sub_u32_e32 v22, v0, v21
	v_mul_i32_i24_e32 v30, 0xa00, v16
	v_mul_i32_i24_e32 v31, 0xa00, v18
	v_mad_i64_i32 v[12:13], s[4:5], v10, s16, v[2:3]
	v_mad_i64_i32 v[14:15], s[4:5], v8, s16, v[2:3]
	v_lshlrev_b64 v[10:11], 12, v[10:11]
	v_lshlrev_b64 v[8:9], 12, v[8:9]
	v_ashrrev_i32_e32 v17, 31, v16
	v_ashrrev_i32_e32 v19, 31, v18
	v_ashrrev_i32_e32 v21, 31, v20
	v_ashrrev_i32_e32 v23, 31, v22
	v_sub_u32_e32 v28, v28, v31
	v_sub_u32_e32 v30, v29, v30
	v_mad_i64_i32 v[24:25], s[4:5], v18, s16, v[2:3]
	v_mad_i64_i32 v[26:27], s[4:5], v16, s16, v[2:3]
	v_lshl_add_u64 v[8:9], s[78:79], 0, v[8:9]
	v_lshl_add_u64 v[10:11], s[78:79], 0, v[10:11]
	v_lshlrev_b64 v[18:19], 12, v[18:19]
	v_lshlrev_b64 v[16:17], 12, v[16:17]
	v_lshlrev_b64 v[32:33], 2, v[20:21]
	v_lshlrev_b64 v[34:35], 2, v[22:23]
	v_ashrrev_i32_e32 v29, 31, v28
	v_ashrrev_i32_e32 v31, 31, v30
	v_lshl_add_u64 v[16:17], s[78:79], 0, v[16:17]
	v_lshl_add_u64 v[18:19], s[78:79], 0, v[18:19]
	v_lshl_add_u64 v[10:11], v[10:11], 0, v[32:33]
	v_lshl_add_u64 v[8:9], v[8:9], 0, v[34:35]
	v_lshl_add_u64 v[14:15], v[14:15], 0, v[34:35]
	v_lshl_add_u64 v[12:13], v[12:13], 0, v[32:33]
	v_lshlrev_b64 v[32:33], 2, v[28:29]
	v_lshlrev_b64 v[34:35], 2, v[30:31]
	v_lshl_add_u64 v[8:9], v[8:9], 0, s[12:13]
	v_cmp_gt_i32_e32 vcc, s15, v22
	v_lshl_add_u64 v[10:11], v[10:11], 0, s[12:13]
	v_lshl_add_u64 v[18:19], v[18:19], 0, v[32:33]
	v_lshl_add_u64 v[16:17], v[16:17], 0, v[34:35]
	v_cmp_gt_i32_e64 s[4:5], s15, v20
	v_lshl_add_u64 v[22:23], v[26:27], 0, v[34:35]
	v_lshl_add_u64 v[24:25], v[24:25], 0, v[32:33]
	v_cndmask_b32_e64 v11, v11, v13, s[4:5]
	v_cndmask_b32_e64 v10, v10, v12, s[4:5]
	v_cndmask_b32_e32 v9, v9, v15, vcc
	v_cndmask_b32_e32 v8, v8, v14, vcc
	v_lshl_add_u64 v[12:13], v[16:17], 0, s[12:13]
	v_cmp_gt_i32_e32 vcc, s15, v30
	v_lshl_add_u64 v[14:15], v[18:19], 0, s[12:13]
	v_cmp_gt_i32_e64 s[4:5], s15, v28
	global_load_dword v194, v[8:9], off
	global_load_dword v195, v[10:11], off
	v_cndmask_b32_e64 v9, v15, v25, s[4:5]
	v_cndmask_b32_e32 v11, v13, v23, vcc
	v_cndmask_b32_e32 v10, v12, v22, vcc
	v_cndmask_b32_e64 v8, v14, v24, s[4:5]
	global_load_dword v196, v[10:11], off
	s_nop 0
	global_load_dword v197, v[8:9], off
	v_add_u32_e32 v6, -2, v6
	s_add_i32 s3, s3, 4
	v_cmp_eq_u32_e32 vcc, 0, v6
	v_mov_b32_e32 v8, s3
	s_or_b64 s[10:11], vcc, s[10:11]
	v_add_u32_e32 v1, 0x800, v1
	v_add_u32_e32 v0, 0x800, v0
	v_mul_hi_i32 v8, v0, s14
	v_mul_hi_i32 v9, v1, s14
	v_add_u32_e32 v28, 0x400, v1
	v_add_u32_e32 v29, 0x400, v0
	v_lshrrev_b32_e32 v10, 31, v8
	v_ashrrev_i32_e32 v8, 10, v8
	v_lshrrev_b32_e32 v11, 31, v9
	v_ashrrev_i32_e32 v9, 10, v9
	v_mul_hi_i32 v12, v29, s14
	v_mul_hi_i32 v13, v28, s14
	v_add_u32_e32 v8, v8, v10
	v_add_u32_e32 v10, v9, v11
	v_lshrrev_b32_e32 v16, 31, v12
	v_ashrrev_i32_e32 v17, 10, v12
	v_lshrrev_b32_e32 v18, 31, v13
	v_ashrrev_i32_e32 v19, 10, v13
	v_mul_i32_i24_e32 v21, 0xa00, v8
	v_mul_i32_i24_e32 v20, 0xa00, v10
	v_add_u32_e32 v16, v17, v16
	v_add_u32_e32 v18, v19, v18
	v_ashrrev_i32_e32 v9, 31, v8
	v_ashrrev_i32_e32 v11, 31, v10
	v_sub_u32_e32 v20, v1, v20
	v_sub_u32_e32 v22, v0, v21
	v_mul_i32_i24_e32 v30, 0xa00, v16
	v_mul_i32_i24_e32 v31, 0xa00, v18
	v_mad_i64_i32 v[12:13], s[4:5], v10, s16, v[2:3]
	v_mad_i64_i32 v[14:15], s[4:5], v8, s16, v[2:3]
	v_lshlrev_b64 v[10:11], 12, v[10:11]
	v_lshlrev_b64 v[8:9], 12, v[8:9]
	v_ashrrev_i32_e32 v17, 31, v16
	v_ashrrev_i32_e32 v19, 31, v18
	v_ashrrev_i32_e32 v21, 31, v20
	v_ashrrev_i32_e32 v23, 31, v22
	v_sub_u32_e32 v28, v28, v31
	v_sub_u32_e32 v30, v29, v30
	v_mad_i64_i32 v[24:25], s[4:5], v18, s16, v[2:3]
	v_mad_i64_i32 v[26:27], s[4:5], v16, s16, v[2:3]
	v_lshl_add_u64 v[8:9], s[78:79], 0, v[8:9]
	v_lshl_add_u64 v[10:11], s[78:79], 0, v[10:11]
	v_lshlrev_b64 v[18:19], 12, v[18:19]
	v_lshlrev_b64 v[16:17], 12, v[16:17]
	v_lshlrev_b64 v[32:33], 2, v[20:21]
	v_lshlrev_b64 v[34:35], 2, v[22:23]
	v_ashrrev_i32_e32 v29, 31, v28
	v_ashrrev_i32_e32 v31, 31, v30
	v_lshl_add_u64 v[16:17], s[78:79], 0, v[16:17]
	v_lshl_add_u64 v[18:19], s[78:79], 0, v[18:19]
	v_lshl_add_u64 v[10:11], v[10:11], 0, v[32:33]
	v_lshl_add_u64 v[8:9], v[8:9], 0, v[34:35]
; DI void prep_phase(const Params& P, const Frame& F, int L) {
;     ...
;     for (int i = F.tid; i < 4 * 2560; i += NTHR) { const int tap = i / 2560, ch = i % 2560;
;         CW[i] = ch < 1536 ? P.in[I_CONV_DN][(size_t)(L * 4 + tap) * 1536 + ch] : P.in[I_CONV_ML][(size_t)(L * 4 + tap) * 1024 + ch - 1536]; }
;     __syncthreads();
	v_lshl_add_u64 v[14:15], v[14:15], 0, v[34:35]
	v_lshl_add_u64 v[12:13], v[12:13], 0, v[32:33]
	v_lshlrev_b64 v[32:33], 2, v[28:29]
	v_lshlrev_b64 v[34:35], 2, v[30:31]
	v_lshl_add_u64 v[8:9], v[8:9], 0, s[12:13]
	v_cmp_gt_i32_e32 vcc, s15, v22
	v_lshl_add_u64 v[10:11], v[10:11], 0, s[12:13]
	v_lshl_add_u64 v[18:19], v[18:19], 0, v[32:33]
	v_lshl_add_u64 v[16:17], v[16:17], 0, v[34:35]
	v_cmp_gt_i32_e64 s[4:5], s15, v20
	v_lshl_add_u64 v[22:23], v[26:27], 0, v[34:35]
	v_lshl_add_u64 v[24:25], v[24:25], 0, v[32:33]
	v_cndmask_b32_e64 v11, v11, v13, s[4:5]
	v_cndmask_b32_e64 v10, v10, v12, s[4:5]
	v_cndmask_b32_e32 v9, v9, v15, vcc
	v_cndmask_b32_e32 v8, v8, v14, vcc
	v_lshl_add_u64 v[12:13], v[16:17], 0, s[12:13]
	v_cmp_gt_i32_e32 vcc, s15, v30
	v_lshl_add_u64 v[14:15], v[18:19], 0, s[12:13]
	v_cmp_gt_i32_e64 s[4:5], s15, v28
	global_load_dword v198, v[8:9], off
	global_load_dword v199, v[10:11], off
	v_cndmask_b32_e64 v9, v15, v25, s[4:5]
	v_cndmask_b32_e32 v11, v13, v23, vcc
	v_cndmask_b32_e32 v10, v12, v22, vcc
	v_cndmask_b32_e64 v8, v14, v24, s[4:5]
	global_load_dword v200, v[10:11], off
	s_nop 0
	global_load_dword v201, v[8:9], off
	v_add_u32_e32 v6, -2, v6
	s_add_i32 s3, s3, 4
	v_cmp_eq_u32_e32 vcc, 0, v6
	v_mov_b32_e32 v8, s3
	s_or_b64 s[10:11], vcc, s[10:11]
	v_add_u32_e32 v1, 0x800, v1
	v_add_u32_e32 v0, 0x800, v0
	v_mul_hi_i32 v8, v0, s14
	v_mul_hi_i32 v9, v1, s14
	v_add_u32_e32 v28, 0x400, v1
	v_add_u32_e32 v29, 0x400, v0
	v_lshrrev_b32_e32 v10, 31, v8
	v_ashrrev_i32_e32 v8, 10, v8
	v_lshrrev_b32_e32 v11, 31, v9
	v_ashrrev_i32_e32 v9, 10, v9
	v_mul_hi_i32 v12, v29, s14
	v_mul_hi_i32 v13, v28, s14
	v_add_u32_e32 v8, v8, v10
	v_add_u32_e32 v10, v9, v11
	v_lshrrev_b32_e32 v16, 31, v12
	v_ashrrev_i32_e32 v17, 10, v12
	v_lshrrev_b32_e32 v18, 31, v13
	v_ashrrev_i32_e32 v19, 10, v13
	v_mul_i32_i24_e32 v21, 0xa00, v8
	v_mul_i32_i24_e32 v20, 0xa00, v10
	v_add_u32_e32 v16, v17, v16
	v_add_u32_e32 v18, v19, v18
	v_ashrrev_i32_e32 v9, 31, v8
	v_ashrrev_i32_e32 v11, 31, v10
	v_sub_u32_e32 v20, v1, v20
	v_sub_u32_e32 v22, v0, v21
	v_mul_i32_i24_e32 v30, 0xa00, v16
	v_mul_i32_i24_e32 v31, 0xa00, v18
	v_mad_i64_i32 v[12:13], s[4:5], v10, s16, v[2:3]
	v_mad_i64_i32 v[14:15], s[4:5], v8, s16, v[2:3]
	v_lshlrev_b64 v[10:11], 12, v[10:11]
	v_lshlrev_b64 v[8:9], 12, v[8:9]
	v_ashrrev_i32_e32 v17, 31, v16
	v_ashrrev_i32_e32 v19, 31, v18
	v_ashrrev_i32_e32 v21, 31, v20
	v_ashrrev_i32_e32 v23, 31, v22
	v_sub_u32_e32 v28, v28, v31
	v_sub_u32_e32 v30, v29, v30
	v_mad_i64_i32 v[24:25], s[4:5], v18, s16, v[2:3]
	v_mad_i64_i32 v[26:27], s[4:5], v16, s16, v[2:3]
	v_lshl_add_u64 v[8:9], s[78:79], 0, v[8:9]
	v_lshl_add_u64 v[10:11], s[78:79], 0, v[10:11]
	v_lshlrev_b64 v[18:19], 12, v[18:19]
	v_lshlrev_b64 v[16:17], 12, v[16:17]
	v_lshlrev_b64 v[32:33], 2, v[20:21]
	v_lshlrev_b64 v[34:35], 2, v[22:23]
	v_ashrrev_i32_e32 v29, 31, v28
	v_ashrrev_i32_e32 v31, 31, v30
	v_lshl_add_u64 v[16:17], s[78:79], 0, v[16:17]
	v_lshl_add_u64 v[18:19], s[78:79], 0, v[18:19]
	v_lshl_add_u64 v[10:11], v[10:11], 0, v[32:33]
	v_lshl_add_u64 v[8:9], v[8:9], 0, v[34:35]
	v_lshl_add_u64 v[14:15], v[14:15], 0, v[34:35]
	v_lshl_add_u64 v[12:13], v[12:13], 0, v[32:33]
	v_lshlrev_b64 v[32:33], 2, v[28:29]
	v_lshlrev_b64 v[34:35], 2, v[30:31]
	v_lshl_add_u64 v[8:9], v[8:9], 0, s[12:13]
	v_cmp_gt_i32_e32 vcc, s15, v22
	v_lshl_add_u64 v[10:11], v[10:11], 0, s[12:13]
	v_lshl_add_u64 v[18:19], v[18:19], 0, v[32:33]
	v_lshl_add_u64 v[16:17], v[16:17], 0, v[34:35]
	v_cmp_gt_i32_e64 s[4:5], s15, v20
	v_lshl_add_u64 v[22:23], v[26:27], 0, v[34:35]
	v_lshl_add_u64 v[24:25], v[24:25], 0, v[32:33]
	v_cndmask_b32_e64 v11, v11, v13, s[4:5]
	v_cndmask_b32_e64 v10, v10, v12, s[4:5]
	v_cndmask_b32_e32 v9, v9, v15, vcc
	v_cndmask_b32_e32 v8, v8, v14, vcc
	v_lshl_add_u64 v[12:13], v[16:17], 0, s[12:13]
	v_cmp_gt_i32_e32 vcc, s15, v30
	v_lshl_add_u64 v[14:15], v[18:19], 0, s[12:13]
	v_cmp_gt_i32_e64 s[4:5], s15, v28
	global_load_dword v202, v[8:9], off
	global_load_dword v203, v[10:11], off
	v_cndmask_b32_e64 v9, v15, v25, s[4:5]
	v_cndmask_b32_e32 v11, v13, v23, vcc
	v_cndmask_b32_e32 v10, v12, v22, vcc
	v_cndmask_b32_e64 v8, v14, v24, s[4:5]
	global_load_dword v204, v[10:11], off
	s_nop 0
	global_load_dword v205, v[8:9], off
	v_add_u32_e32 v6, -2, v6
	s_add_i32 s3, s3, 4
	v_cmp_eq_u32_e32 vcc, 0, v6
	v_mov_b32_e32 v8, s3
	s_or_b64 s[10:11], vcc, s[10:11]
	v_add_u32_e32 v1, 0x800, v1
	v_add_u32_e32 v0, 0x800, v0
	s_waitcnt vmcnt(18)
	ds_write2st64_b32 v7, v186, v187 offset1:8
	s_waitcnt vmcnt(16)
	ds_write2st64_b32 v7, v188, v189 offset0:16 offset1:24
	v_add_u32_e32 v7, 0x2000, v7
	s_waitcnt vmcnt(14)
	ds_write2st64_b32 v7, v190, v191 offset1:8
	s_waitcnt vmcnt(12)
	ds_write2st64_b32 v7, v192, v193 offset0:16 offset1:24
	v_add_u32_e32 v7, 0x2000, v7
	s_waitcnt vmcnt(10)
	ds_write2st64_b32 v7, v194, v195 offset1:8
	s_waitcnt vmcnt(8)
	ds_write2st64_b32 v7, v196, v197 offset0:16 offset1:24
	v_add_u32_e32 v7, 0x2000, v7
	s_waitcnt vmcnt(6)
	ds_write2st64_b32 v7, v198, v199 offset1:8
	s_waitcnt vmcnt(4)
	ds_write2st64_b32 v7, v200, v201 offset0:16 offset1:24
	v_add_u32_e32 v7, 0x2000, v7
	s_waitcnt vmcnt(2)
	ds_write2st64_b32 v7, v202, v203 offset1:8
	s_waitcnt vmcnt(0)
	ds_write2st64_b32 v7, v204, v205 offset0:16 offset1:24
	v_add_u32_e32 v7, 0x2000, v7
	s_or_b64 exec, exec, s[10:11]
	v_lshlrev_b32_e32 v2, 9, v8

.LBB0_1017:
	s_cmp_lt_u32 s3, 0x40001
	s_mov_b64 s[18:19], 0
	s_cselect_b64 s[20:21], -1, 0
	s_mov_b64 s[22:23], -1
	s_and_b64 vcc, exec, s[20:21]
	s_cbranch_vccnz .LBB0_1014
	s_branch .LBB0_1011
	s_nop 0
	s_nop 0
	s_nop 0
	s_nop 0
	s_nop 0
	s_nop 0
	s_nop 0
	s_nop 0
	s_nop 0
	s_nop 0
	s_nop 0
	s_nop 0
	s_nop 0
	s_nop 0
	s_nop 0
	s_nop 0
	s_nop 0
	s_nop 0
	s_nop 0
	s_nop 0
.LBB0_1018:
	s_or_b64 exec, exec, s[14:15]
	s_and_b64 s[14:15], s[16:17], exec

; DI void prep_phase(const Params& P, const Frame& F, int L) {
;     ...
;     for (int i = F.tid; i < 4 * 2560; i += NTHR) { const int tap = i / 2560, ch = i % 2560;
;         CW[i] = ch < 1536 ? P.in[I_CONV_DN][(size_t)(L * 4 + tap) * 1536 + ch] : P.in[I_CONV_ML][(size_t)(L * 4 + tap) * 1024 + ch - 1536]; }
.LBB0_1861:
	v_mul_hi_i32 v8, v0, s14
	v_mul_hi_i32 v9, v1, s14
	v_add_u32_e32 v21, 0x400, v1
	v_add_u32_e32 v23, 0x400, v0
	v_lshrrev_b32_e32 v10, 31, v8
	v_ashrrev_i32_e32 v8, 10, v8
	v_lshrrev_b32_e32 v11, 31, v9
	v_ashrrev_i32_e32 v9, 10, v9
	v_mul_hi_i32 v12, v23, s14
	v_mul_hi_i32 v13, v21, s14
	v_add_u32_e32 v10, v8, v10
	v_add_u32_e32 v8, v9, v11
	v_lshrrev_b32_e32 v9, 31, v12
	v_ashrrev_i32_e32 v11, 10, v12
	v_lshrrev_b32_e32 v12, 31, v13
	v_ashrrev_i32_e32 v13, 10, v13
	v_mul_i32_i24_e32 v14, 0xa00, v10
	v_mul_i32_i24_e32 v15, 0xa00, v8
	v_add_u32_e32 v8, 4, v8
	v_add_u32_e32 v10, 4, v10
	v_add_u32_e32 v22, v11, v9
	v_add_u32_e32 v13, v13, v12
	v_sub_u32_e32 v12, v1, v15
	v_sub_u32_e32 v14, v0, v14
	v_ashrrev_i32_e32 v11, 31, v10
	v_ashrrev_i32_e32 v9, 31, v8
	v_mul_i32_i24_e32 v25, 0xa00, v22
	v_mul_i32_i24_e32 v24, 0xa00, v13
	v_add_u32_e32 v20, 4, v13
	v_add_u32_e32 v22, 4, v22
	v_mad_i64_i32 v[16:17], s[4:5], v8, s16, v[2:3]
	v_mad_i64_i32 v[18:19], s[4:5], v10, s16, v[2:3]
	v_lshlrev_b64 v[8:9], 12, v[8:9]
	v_lshlrev_b64 v[10:11], 12, v[10:11]
	v_ashrrev_i32_e32 v13, 31, v12
	v_ashrrev_i32_e32 v15, 31, v14
	v_sub_u32_e32 v24, v21, v24
	v_sub_u32_e32 v26, v23, v25
	v_ashrrev_i32_e32 v23, 31, v22
	v_ashrrev_i32_e32 v21, 31, v20
	v_mad_i64_i32 v[28:29], s[4:5], v20, s16, v[2:3]
	v_mad_i64_i32 v[30:31], s[4:5], v22, s16, v[2:3]
	v_lshl_add_u64 v[10:11], s[78:79], 0, v[10:11]
	v_lshl_add_u64 v[8:9], s[78:79], 0, v[8:9]
	s_waitcnt vmcnt(15)
	v_lshlrev_b64 v[32:33], 2, v[12:13]
	v_lshlrev_b64 v[34:35], 2, v[14:15]
	v_lshlrev_b64 v[20:21], 12, v[20:21]
	v_lshlrev_b64 v[22:23], 12, v[22:23]
	v_ashrrev_i32_e32 v25, 31, v24
	v_ashrrev_i32_e32 v27, 31, v26
	v_lshl_add_u64 v[8:9], v[8:9], 0, v[32:33]
	v_lshl_add_u64 v[10:11], v[10:11], 0, v[34:35]
	v_lshl_add_u64 v[18:19], v[18:19], 0, v[34:35]
	v_lshl_add_u64 v[16:17], v[16:17], 0, v[32:33]
	v_lshl_add_u64 v[22:23], s[78:79], 0, v[22:23]
	v_lshl_add_u64 v[20:21], s[78:79], 0, v[20:21]
	v_lshlrev_b64 v[32:33], 2, v[24:25]
	v_lshlrev_b64 v[34:35], 2, v[26:27]
	v_lshl_add_u64 v[10:11], v[10:11], 0, s[12:13]
	v_cmp_gt_i32_e32 vcc, s15, v14
	v_lshl_add_u64 v[8:9], v[8:9], 0, s[12:13]
	v_lshl_add_u64 v[14:15], v[20:21], 0, v[32:33]
	v_lshl_add_u64 v[20:21], v[22:23], 0, v[34:35]
	v_cmp_gt_i32_e64 s[4:5], s15, v12
	v_lshl_add_u64 v[22:23], v[30:31], 0, v[34:35]
	v_lshl_add_u64 v[28:29], v[28:29], 0, v[32:33]
	v_cndmask_b32_e64 v9, v9, v17, s[4:5]
	v_cndmask_b32_e64 v8, v8, v16, s[4:5]
	v_cndmask_b32_e32 v11, v11, v19, vcc
	v_cndmask_b32_e32 v10, v10, v18, vcc
	v_lshl_add_u64 v[12:13], v[20:21], 0, s[12:13]
	v_cmp_gt_i32_e32 vcc, s15, v26
	v_lshl_add_u64 v[14:15], v[14:15], 0, s[12:13]
	v_cmp_gt_i32_e64 s[4:5], s15, v24
	global_load_dword v186, v[10:11], off
	global_load_dword v187, v[8:9], off
	v_cndmask_b32_e64 v9, v15, v29, s[4:5]
	v_cndmask_b32_e32 v11, v13, v23, vcc
	v_cndmask_b32_e32 v10, v12, v22, vcc
	v_cndmask_b32_e64 v8, v14, v28, s[4:5]
	global_load_dword v188, v[10:11], off
	s_nop 0
	global_load_dword v189, v[8:9], off
	v_add_u32_e32 v6, -2, v6
	s_add_i32 s3, s3, 4
	v_cmp_eq_u32_e32 vcc, 0, v6
	v_mov_b32_e32 v8, s3
	s_or_b64 s[10:11], vcc, s[10:11]
	v_add_u32_e32 v1, 0x800, v1
	v_add_u32_e32 v0, 0x800, v0
	v_mul_hi_i32 v8, v0, s14
	v_mul_hi_i32 v9, v1, s14
	v_add_u32_e32 v21, 0x400, v1
	v_add_u32_e32 v23, 0x400, v0
	v_lshrrev_b32_e32 v10, 31, v8
	v_ashrrev_i32_e32 v8, 10, v8
	v_lshrrev_b32_e32 v11, 31, v9
	v_ashrrev_i32_e32 v9, 10, v9
	v_mul_hi_i32 v12, v23, s14
	v_mul_hi_i32 v13, v21, s14
	v_add_u32_e32 v10, v8, v10
	v_add_u32_e32 v8, v9, v11
	v_lshrrev_b32_e32 v9, 31, v12
	v_ashrrev_i32_e32 v11, 10, v12
	v_lshrrev_b32_e32 v12, 31, v13
	v_ashrrev_i32_e32 v13, 10, v13
	v_mul_i32_i24_e32 v14, 0xa00, v10
	v_mul_i32_i24_e32 v15, 0xa00, v8
	v_add_u32_e32 v8, 4, v8
	v_add_u32_e32 v10, 4, v10
	v_add_u32_e32 v22, v11, v9
	v_add_u32_e32 v13, v13, v12
	v_sub_u32_e32 v12, v1, v15
	v_sub_u32_e32 v14, v0, v14
	v_ashrrev_i32_e32 v11, 31, v10
	v_ashrrev_i32_e32 v9, 31, v8
	v_mul_i32_i24_e32 v25, 0xa00, v22
	v_mul_i32_i24_e32 v24, 0xa00, v13
	v_add_u32_e32 v20, 4, v13
	v_add_u32_e32 v22, 4, v22
	v_mad_i64_i32 v[16:17], s[4:5], v8, s16, v[2:3]
	v_mad_i64_i32 v[18:19], s[4:5], v10, s16, v[2:3]
	v_lshlrev_b64 v[8:9], 12, v[8:9]
	v_lshlrev_b64 v[10:11], 12, v[10:11]
	v_ashrrev_i32_e32 v13, 31, v12
	v_ashrrev_i32_e32 v15, 31, v14
	v_sub_u32_e32 v24, v21, v24
	v_sub_u32_e32 v26, v23, v25
	v_ashrrev_i32_e32 v23, 31, v22
	v_ashrrev_i32_e32 v21, 31, v20
	v_mad_i64_i32 v[28:29], s[4:5], v20, s16, v[2:3]
	v_mad_i64_i32 v[30:31], s[4:5], v22, s16, v[2:3]
	v_lshl_add_u64 v[10:11], s[78:79], 0, v[10:11]
	v_lshl_add_u64 v[8:9], s[78:79], 0, v[8:9]
	v_lshlrev_b64 v[32:33], 2, v[12:13]
	v_lshlrev_b64 v[34:35], 2, v[14:15]
	v_lshlrev_b64 v[20:21], 12, v[20:21]
	v_lshlrev_b64 v[22:23], 12, v[22:23]
	v_ashrrev_i32_e32 v25, 31, v24
	v_ashrrev_i32_e32 v27, 31, v26
	v_lshl_add_u64 v[8:9], v[8:9], 0, v[32:33]
	v_lshl_add_u64 v[10:11], v[10:11], 0, v[34:35]
	v_lshl_add_u64 v[18:19], v[18:19], 0, v[34:35]
	v_lshl_add_u64 v[16:17], v[16:17], 0, v[32:33]
	v_lshl_add_u64 v[22:23], s[78:79], 0, v[22:23]
	v_lshl_add_u64 v[20:21], s[78:79], 0, v[20:21]
	v_lshlrev_b64 v[32:33], 2, v[24:25]
	v_lshlrev_b64 v[34:35], 2, v[26:27]
	v_lshl_add_u64 v[10:11], v[10:11], 0, s[12:13]
	v_cmp_gt_i32_e32 vcc, s15, v14
	v_lshl_add_u64 v[8:9], v[8:9], 0, s[12:13]
	v_lshl_add_u64 v[14:15], v[20:21], 0, v[32:33]
	v_lshl_add_u64 v[20:21], v[22:23], 0, v[34:35]
	v_cmp_gt_i32_e64 s[4:5], s15, v12
	v_lshl_add_u64 v[22:23], v[30:31], 0, v[34:35]
	v_lshl_add_u64 v[28:29], v[28:29], 0, v[32:33]
	v_cndmask_b32_e64 v9, v9, v17, s[4:5]
; DI void prep_phase(const Params& P, const Frame& F, int L) {
;     ...
;     for (int i = F.tid; i < 4 * 2560; i += NTHR) { const int tap = i / 2560, ch = i % 2560;
;         CW[i] = ch < 1536 ? P.in[I_CONV_DN][(size_t)(L * 4 + tap) * 1536 + ch] : P.in[I_CONV_ML][(size_t)(L * 4 + tap) * 1024 + ch - 1536]; }
	v_cndmask_b32_e64 v8, v8, v16, s[4:5]
	v_cndmask_b32_e32 v11, v11, v19, vcc
	v_cndmask_b32_e32 v10, v10, v18, vcc
	v_lshl_add_u64 v[12:13], v[20:21], 0, s[12:13]
	v_cmp_gt_i32_e32 vcc, s15, v26
	v_lshl_add_u64 v[14:15], v[14:15], 0, s[12:13]
	v_cmp_gt_i32_e64 s[4:5], s15, v24
	global_load_dword v190, v[10:11], off
	global_load_dword v191, v[8:9], off
	v_cndmask_b32_e64 v9, v15, v29, s[4:5]
	v_cndmask_b32_e32 v11, v13, v23, vcc
	v_cndmask_b32_e32 v10, v12, v22, vcc
	v_cndmask_b32_e64 v8, v14, v28, s[4:5]
	global_load_dword v192, v[10:11], off
	s_nop 0
	global_load_dword v193, v[8:9], off
	v_add_u32_e32 v6, -2, v6
	s_add_i32 s3, s3, 4
	v_cmp_eq_u32_e32 vcc, 0, v6
	v_mov_b32_e32 v8, s3
	s_or_b64 s[10:11], vcc, s[10:11]
	v_add_u32_e32 v1, 0x800, v1
	v_add_u32_e32 v0, 0x800, v0
	v_mul_hi_i32 v8, v0, s14
	v_mul_hi_i32 v9, v1, s14
	v_add_u32_e32 v21, 0x400, v1
	v_add_u32_e32 v23, 0x400, v0
	v_lshrrev_b32_e32 v10, 31, v8
	v_ashrrev_i32_e32 v8, 10, v8
	v_lshrrev_b32_e32 v11, 31, v9
	v_ashrrev_i32_e32 v9, 10, v9
	v_mul_hi_i32 v12, v23, s14
	v_mul_hi_i32 v13, v21, s14
	v_add_u32_e32 v10, v8, v10
	v_add_u32_e32 v8, v9, v11
	v_lshrrev_b32_e32 v9, 31, v12
	v_ashrrev_i32_e32 v11, 10, v12
	v_lshrrev_b32_e32 v12, 31, v13
	v_ashrrev_i32_e32 v13, 10, v13
	v_mul_i32_i24_e32 v14, 0xa00, v10
	v_mul_i32_i24_e32 v15, 0xa00, v8
	v_add_u32_e32 v8, 4, v8
	v_add_u32_e32 v10, 4, v10
	v_add_u32_e32 v22, v11, v9
	v_add_u32_e32 v13, v13, v12
	v_sub_u32_e32 v12, v1, v15
	v_sub_u32_e32 v14, v0, v14
	v_ashrrev_i32_e32 v11, 31, v10
	v_ashrrev_i32_e32 v9, 31, v8
	v_mul_i32_i24_e32 v25, 0xa00, v22
	v_mul_i32_i24_e32 v24, 0xa00, v13
	v_add_u32_e32 v20, 4, v13
	v_add_u32_e32 v22, 4, v22
	v_mad_i64_i32 v[16:17], s[4:5], v8, s16, v[2:3]
	v_mad_i64_i32 v[18:19], s[4:5], v10, s16, v[2:3]
	v_lshlrev_b64 v[8:9], 12, v[8:9]
	v_lshlrev_b64 v[10:11], 12, v[10:11]
	v_ashrrev_i32_e32 v13, 31, v12
	v_ashrrev_i32_e32 v15, 31, v14
	v_sub_u32_e32 v24, v21, v24
	v_sub_u32_e32 v26, v23, v25
	v_ashrrev_i32_e32 v23, 31, v22
	v_ashrrev_i32_e32 v21, 31, v20
	v_mad_i64_i32 v[28:29], s[4:5], v20, s16, v[2:3]
	v_mad_i64_i32 v[30:31], s[4:5], v22, s16, v[2:3]
	v_lshl_add_u64 v[10:11], s[78:79], 0, v[10:11]
	v_lshl_add_u64 v[8:9], s[78:79], 0, v[8:9]
	v_lshlrev_b64 v[32:33], 2, v[12:13]
	v_lshlrev_b64 v[34:35], 2, v[14:15]
	v_lshlrev_b64 v[20:21], 12, v[20:21]
	v_lshlrev_b64 v[22:23], 12, v[22:23]
	v_ashrrev_i32_e32 v25, 31, v24
	v_ashrrev_i32_e32 v27, 31, v26
	v_lshl_add_u64 v[8:9], v[8:9], 0, v[32:33]
	v_lshl_add_u64 v[10:11], v[10:11], 0, v[34:35]
	v_lshl_add_u64 v[18:19], v[18:19], 0, v[34:35]
	v_lshl_add_u64 v[16:17], v[16:17], 0, v[32:33]
	v_lshl_add_u64 v[22:23], s[78:79], 0, v[22:23]
	v_lshl_add_u64 v[20:21], s[78:79], 0, v[20:21]
	v_lshlrev_b64 v[32:33], 2, v[24:25]
	v_lshlrev_b64 v[34:35], 2, v[26:27]
	v_lshl_add_u64 v[10:11], v[10:11], 0, s[12:13]
	v_cmp_gt_i32_e32 vcc, s15, v14
	v_lshl_add_u64 v[8:9], v[8:9], 0, s[12:13]
	v_lshl_add_u64 v[14:15], v[20:21], 0, v[32:33]
	v_lshl_add_u64 v[20:21], v[22:23], 0, v[34:35]
	v_cmp_gt_i32_e64 s[4:5], s15, v12
	v_lshl_add_u64 v[22:23], v[30:31], 0, v[34:35]
	v_lshl_add_u64 v[28:29], v[28:29], 0, v[32:33]
	v_cndmask_b32_e64 v9, v9, v17, s[4:5]
	v_cndmask_b32_e64 v8, v8, v16, s[4:5]
	v_cndmask_b32_e32 v11, v11, v19, vcc
	v_cndmask_b32_e32 v10, v10, v18, vcc
	v_lshl_add_u64 v[12:13], v[20:21], 0, s[12:13]
	v_cmp_gt_i32_e32 vcc, s15, v26
	v_lshl_add_u64 v[14:15], v[14:15], 0, s[12:13]
	v_cmp_gt_i32_e64 s[4:5], s15, v24
	global_load_dword v194, v[10:11], off
	global_load_dword v195, v[8:9], off
	v_cndmask_b32_e64 v9, v15, v29, s[4:5]
	v_cndmask_b32_e32 v11, v13, v23, vcc
	v_cndmask_b32_e32 v10, v12, v22, vcc
	v_cndmask_b32_e64 v8, v14, v28, s[4:5]
	global_load_dword v196, v[10:11], off
	s_nop 0
	global_load_dword v197, v[8:9], off
	v_add_u32_e32 v6, -2, v6
	s_add_i32 s3, s3, 4
	v_cmp_eq_u32_e32 vcc, 0, v6
	v_mov_b32_e32 v8, s3
	s_or_b64 s[10:11], vcc, s[10:11]
	v_add_u32_e32 v1, 0x800, v1
	v_add_u32_e32 v0, 0x800, v0
	v_mul_hi_i32 v8, v0, s14
	v_mul_hi_i32 v9, v1, s14
	v_add_u32_e32 v21, 0x400, v1
	v_add_u32_e32 v23, 0x400, v0
	v_lshrrev_b32_e32 v10, 31, v8
	v_ashrrev_i32_e32 v8, 10, v8
	v_lshrrev_b32_e32 v11, 31, v9
	v_ashrrev_i32_e32 v9, 10, v9
	v_mul_hi_i32 v12, v23, s14
	v_mul_hi_i32 v13, v21, s14
	v_add_u32_e32 v10, v8, v10
	v_add_u32_e32 v8, v9, v11
	v_lshrrev_b32_e32 v9, 31, v12
	v_ashrrev_i32_e32 v11, 10, v12
	v_lshrrev_b32_e32 v12, 31, v13
	v_ashrrev_i32_e32 v13, 10, v13
	v_mul_i32_i24_e32 v14, 0xa00, v10
	v_mul_i32_i24_e32 v15, 0xa00, v8
	v_add_u32_e32 v8, 4, v8
	v_add_u32_e32 v10, 4, v10
	v_add_u32_e32 v22, v11, v9
	v_add_u32_e32 v13, v13, v12
	v_sub_u32_e32 v12, v1, v15
	v_sub_u32_e32 v14, v0, v14
	v_ashrrev_i32_e32 v11, 31, v10
	v_ashrrev_i32_e32 v9, 31, v8
	v_mul_i32_i24_e32 v25, 0xa00, v22
	v_mul_i32_i24_e32 v24, 0xa00, v13
	v_add_u32_e32 v20, 4, v13
	v_add_u32_e32 v22, 4, v22
	v_mad_i64_i32 v[16:17], s[4:5], v8, s16, v[2:3]
	v_mad_i64_i32 v[18:19], s[4:5], v10, s16, v[2:3]
	v_lshlrev_b64 v[8:9], 12, v[8:9]
	v_lshlrev_b64 v[10:11], 12, v[10:11]
	v_ashrrev_i32_e32 v13, 31, v12
	v_ashrrev_i32_e32 v15, 31, v14
	v_sub_u32_e32 v24, v21, v24
	v_sub_u32_e32 v26, v23, v25
	v_ashrrev_i32_e32 v23, 31, v22
	v_ashrrev_i32_e32 v21, 31, v20
	v_mad_i64_i32 v[28:29], s[4:5], v20, s16, v[2:3]
	v_mad_i64_i32 v[30:31], s[4:5], v22, s16, v[2:3]
	v_lshl_add_u64 v[10:11], s[78:79], 0, v[10:11]
	v_lshl_add_u64 v[8:9], s[78:79], 0, v[8:9]
	v_lshlrev_b64 v[32:33], 2, v[12:13]
	v_lshlrev_b64 v[34:35], 2, v[14:15]
	v_lshlrev_b64 v[20:21], 12, v[20:21]
	v_lshlrev_b64 v[22:23], 12, v[22:23]
	v_ashrrev_i32_e32 v25, 31, v24
	v_ashrrev_i32_e32 v27, 31, v26
; DI void prep_phase(const Params& P, const Frame& F, int L) {
;     ...
;     for (int i = F.tid; i < 4 * 2560; i += NTHR) { const int tap = i / 2560, ch = i % 2560;
;         CW[i] = ch < 1536 ? P.in[I_CONV_DN][(size_t)(L * 4 + tap) * 1536 + ch] : P.in[I_CONV_ML][(size_t)(L * 4 + tap) * 1024 + ch - 1536]; }
;     __syncthreads();
	v_lshl_add_u64 v[8:9], v[8:9], 0, v[32:33]
	v_lshl_add_u64 v[10:11], v[10:11], 0, v[34:35]
	v_lshl_add_u64 v[18:19], v[18:19], 0, v[34:35]
	v_lshl_add_u64 v[16:17], v[16:17], 0, v[32:33]
	v_lshl_add_u64 v[22:23], s[78:79], 0, v[22:23]
	v_lshl_add_u64 v[20:21], s[78:79], 0, v[20:21]
	v_lshlrev_b64 v[32:33], 2, v[24:25]
	v_lshlrev_b64 v[34:35], 2, v[26:27]
	v_lshl_add_u64 v[10:11], v[10:11], 0, s[12:13]
	v_cmp_gt_i32_e32 vcc, s15, v14
	v_lshl_add_u64 v[8:9], v[8:9], 0, s[12:13]
	v_lshl_add_u64 v[14:15], v[20:21], 0, v[32:33]
	v_lshl_add_u64 v[20:21], v[22:23], 0, v[34:35]
	v_cmp_gt_i32_e64 s[4:5], s15, v12
	v_lshl_add_u64 v[22:23], v[30:31], 0, v[34:35]
	v_lshl_add_u64 v[28:29], v[28:29], 0, v[32:33]
	v_cndmask_b32_e64 v9, v9, v17, s[4:5]
	v_cndmask_b32_e64 v8, v8, v16, s[4:5]
	v_cndmask_b32_e32 v11, v11, v19, vcc
	v_cndmask_b32_e32 v10, v10, v18, vcc
	v_lshl_add_u64 v[12:13], v[20:21], 0, s[12:13]
	v_cmp_gt_i32_e32 vcc, s15, v26
	v_lshl_add_u64 v[14:15], v[14:15], 0, s[12:13]
	v_cmp_gt_i32_e64 s[4:5], s15, v24
	global_load_dword v198, v[10:11], off
	global_load_dword v199, v[8:9], off
	v_cndmask_b32_e64 v9, v15, v29, s[4:5]
	v_cndmask_b32_e32 v11, v13, v23, vcc
	v_cndmask_b32_e32 v10, v12, v22, vcc
	v_cndmask_b32_e64 v8, v14, v28, s[4:5]
	global_load_dword v200, v[10:11], off
	s_nop 0
	global_load_dword v201, v[8:9], off
	v_add_u32_e32 v6, -2, v6
	s_add_i32 s3, s3, 4
	v_cmp_eq_u32_e32 vcc, 0, v6
	v_mov_b32_e32 v8, s3
	s_or_b64 s[10:11], vcc, s[10:11]
	v_add_u32_e32 v1, 0x800, v1
	v_add_u32_e32 v0, 0x800, v0
	v_mul_hi_i32 v8, v0, s14
	v_mul_hi_i32 v9, v1, s14
	v_add_u32_e32 v21, 0x400, v1
	v_add_u32_e32 v23, 0x400, v0
	v_lshrrev_b32_e32 v10, 31, v8
	v_ashrrev_i32_e32 v8, 10, v8
	v_lshrrev_b32_e32 v11, 31, v9
	v_ashrrev_i32_e32 v9, 10, v9
	v_mul_hi_i32 v12, v23, s14
	v_mul_hi_i32 v13, v21, s14
	v_add_u32_e32 v10, v8, v10
	v_add_u32_e32 v8, v9, v11
	v_lshrrev_b32_e32 v9, 31, v12
	v_ashrrev_i32_e32 v11, 10, v12
	v_lshrrev_b32_e32 v12, 31, v13
	v_ashrrev_i32_e32 v13, 10, v13
	v_mul_i32_i24_e32 v14, 0xa00, v10
	v_mul_i32_i24_e32 v15, 0xa00, v8
	v_add_u32_e32 v8, 4, v8
	v_add_u32_e32 v10, 4, v10
	v_add_u32_e32 v22, v11, v9
	v_add_u32_e32 v13, v13, v12
	v_sub_u32_e32 v12, v1, v15
	v_sub_u32_e32 v14, v0, v14
	v_ashrrev_i32_e32 v11, 31, v10
	v_ashrrev_i32_e32 v9, 31, v8
	v_mul_i32_i24_e32 v25, 0xa00, v22
	v_mul_i32_i24_e32 v24, 0xa00, v13
	v_add_u32_e32 v20, 4, v13
	v_add_u32_e32 v22, 4, v22
	v_mad_i64_i32 v[16:17], s[4:5], v8, s16, v[2:3]
	v_mad_i64_i32 v[18:19], s[4:5], v10, s16, v[2:3]
	v_lshlrev_b64 v[8:9], 12, v[8:9]
	v_lshlrev_b64 v[10:11], 12, v[10:11]
	v_ashrrev_i32_e32 v13, 31, v12
	v_ashrrev_i32_e32 v15, 31, v14
	v_sub_u32_e32 v24, v21, v24
	v_sub_u32_e32 v26, v23, v25
	v_ashrrev_i32_e32 v23, 31, v22
	v_ashrrev_i32_e32 v21, 31, v20
	v_mad_i64_i32 v[28:29], s[4:5], v20, s16, v[2:3]
	v_mad_i64_i32 v[30:31], s[4:5], v22, s16, v[2:3]
	v_lshl_add_u64 v[10:11], s[78:79], 0, v[10:11]
	v_lshl_add_u64 v[8:9], s[78:79], 0, v[8:9]
	v_lshlrev_b64 v[32:33], 2, v[12:13]
	v_lshlrev_b64 v[34:35], 2, v[14:15]
	v_lshlrev_b64 v[20:21], 12, v[20:21]
	v_lshlrev_b64 v[22:23], 12, v[22:23]
	v_ashrrev_i32_e32 v25, 31, v24
	v_ashrrev_i32_e32 v27, 31, v26
	v_lshl_add_u64 v[8:9], v[8:9], 0, v[32:33]
	v_lshl_add_u64 v[10:11], v[10:11], 0, v[34:35]
	v_lshl_add_u64 v[18:19], v[18:19], 0, v[34:35]
	v_lshl_add_u64 v[16:17], v[16:17], 0, v[32:33]
	v_lshl_add_u64 v[22:23], s[78:79], 0, v[22:23]
	v_lshl_add_u64 v[20:21], s[78:79], 0, v[20:21]
	v_lshlrev_b64 v[32:33], 2, v[24:25]
	v_lshlrev_b64 v[34:35], 2, v[26:27]
	v_lshl_add_u64 v[10:11], v[10:11], 0, s[12:13]
	v_cmp_gt_i32_e32 vcc, s15, v14
	v_lshl_add_u64 v[8:9], v[8:9], 0, s[12:13]
	v_lshl_add_u64 v[14:15], v[20:21], 0, v[32:33]
	v_lshl_add_u64 v[20:21], v[22:23], 0, v[34:35]
	v_cmp_gt_i32_e64 s[4:5], s15, v12
	v_lshl_add_u64 v[22:23], v[30:31], 0, v[34:35]
	v_lshl_add_u64 v[28:29], v[28:29], 0, v[32:33]
	v_cndmask_b32_e64 v9, v9, v17, s[4:5]
	v_cndmask_b32_e64 v8, v8, v16, s[4:5]
	v_cndmask_b32_e32 v11, v11, v19, vcc
	v_cndmask_b32_e32 v10, v10, v18, vcc
	v_lshl_add_u64 v[12:13], v[20:21], 0, s[12:13]
	v_cmp_gt_i32_e32 vcc, s15, v26
	v_lshl_add_u64 v[14:15], v[14:15], 0, s[12:13]
	v_cmp_gt_i32_e64 s[4:5], s15, v24
	global_load_dword v202, v[10:11], off
	global_load_dword v203, v[8:9], off
	v_cndmask_b32_e64 v9, v15, v29, s[4:5]
	v_cndmask_b32_e32 v11, v13, v23, vcc
	v_cndmask_b32_e32 v10, v12, v22, vcc
	v_cndmask_b32_e64 v8, v14, v28, s[4:5]
	global_load_dword v204, v[10:11], off
	s_nop 0
	global_load_dword v205, v[8:9], off
	v_add_u32_e32 v6, -2, v6
	s_add_i32 s3, s3, 4
	v_cmp_eq_u32_e32 vcc, 0, v6
	v_mov_b32_e32 v8, s3
	s_or_b64 s[10:11], vcc, s[10:11]
	v_add_u32_e32 v1, 0x800, v1
	v_add_u32_e32 v0, 0x800, v0
	s_waitcnt vmcnt(18)
	ds_write2st64_b32 v7, v186, v187 offset1:8
	s_waitcnt vmcnt(16)
	ds_write2st64_b32 v7, v188, v189 offset0:16 offset1:24
	v_add_u32_e32 v7, 0x2000, v7
	s_waitcnt vmcnt(14)
	ds_write2st64_b32 v7, v190, v191 offset1:8
	s_waitcnt vmcnt(12)
	ds_write2st64_b32 v7, v192, v193 offset0:16 offset1:24
	v_add_u32_e32 v7, 0x2000, v7
	s_waitcnt vmcnt(10)
	ds_write2st64_b32 v7, v194, v195 offset1:8
	s_waitcnt vmcnt(8)
	ds_write2st64_b32 v7, v196, v197 offset0:16 offset1:24
	v_add_u32_e32 v7, 0x2000, v7
	s_waitcnt vmcnt(6)
	ds_write2st64_b32 v7, v198, v199 offset1:8
	s_waitcnt vmcnt(4)
	ds_write2st64_b32 v7, v200, v201 offset0:16 offset1:24
	v_add_u32_e32 v7, 0x2000, v7
	s_waitcnt vmcnt(2)
	ds_write2st64_b32 v7, v202, v203 offset1:8
	s_waitcnt vmcnt(0)
	ds_write2st64_b32 v7, v204, v205 offset0:16 offset1:24
	v_add_u32_e32 v7, 0x2000, v7
	s_or_b64 exec, exec, s[10:11]
	v_lshlrev_b32_e32 v2, 9, v8

.LBB0_2582:
	s_cmp_lt_u32 s3, 0x40001
	s_mov_b64 s[18:19], 0
	s_cselect_b64 s[20:21], -1, 0
	s_mov_b64 s[22:23], -1
	s_and_b64 vcc, exec, s[20:21]
	s_cbranch_vccnz .LBB0_2579
	s_branch .LBB0_2576
	s_nop 0
.LBB0_2583:
	s_or_b64 exec, exec, s[14:15]
	s_and_b64 s[14:15], s[16:17], exec
